# write-through (sc0 sc1) stores also for qT (Q GEMM epilogue)
# speedup vs baseline: 1.0162x; 1.0100x over previous
.LBB3_27:
	s_lshl_b32 s0, s69, 8
	s_ashr_i32 s1, s0, 31
	s_lshl_b64 s[4:5], s[0:1], 2
	v_or_b32_e32 v147, s80, v148
	s_waitcnt lgkmcnt(0)
	s_add_u32 s4, s26, s4
	s_addc_u32 s5, s27, s5
	v_lshlrev_b32_e32 v66, 2, v147
	s_barrier
	global_load_dwordx4 v[142:145], v66, s[4:5]
	global_load_dwordx4 v[138:141], v66, s[4:5] offset:16
	global_load_dwordx4 v[134:137], v66, s[4:5] offset:512
	s_nop 0
	global_load_dwordx4 v[66:69], v66, s[4:5] offset:528
	s_movk_i32 s3, 0x210
	v_mul_lo_u32 v1, v1, s3
	v_lshl_add_u32 v1, v147, 1, v1
	v_bfe_u32 v146, v0, 5, 1
	v_and_b32_e32 v148, 31, v0
	v_lshl_or_b32 v170, s57, 4, v146
	v_lshlrev_b32_e32 v146, 4, v148
	v_mad_u64_u32 v[148:149], s[4:5], v170, s3, v[146:147]
	s_lshl_b32 s3, s67, 8
	s_lshl_b64 s[0:1], s[0:1], 1
	v_mov_b32_e32 v147, 0
	s_waitcnt vmcnt(0)
	v_pk_add_f32 v[132:133], v[132:133], v[144:145]
	v_pk_add_f32 v[130:131], v[130:131], v[142:143]
	v_pk_add_f32 v[128:129], v[128:129], v[140:141]
	v_pk_add_f32 v[126:127], v[126:127], v[138:139]
	v_pk_add_f32 v[124:125], v[124:125], v[136:137]
	v_pk_add_f32 v[122:123], v[122:123], v[134:135]
	v_pk_add_f32 v[116:117], v[116:117], v[68:69]
	v_pk_add_f32 v[114:115], v[114:115], v[66:67]
	v_pk_add_f32 v[120:121], v[120:121], v[144:145]
	v_pk_add_f32 v[118:119], v[118:119], v[142:143]
	v_pk_add_f32 v[112:113], v[112:113], v[140:141]
	v_pk_add_f32 v[110:111], v[110:111], v[138:139]
	v_pk_add_f32 v[108:109], v[108:109], v[136:137]
	v_pk_add_f32 v[106:107], v[106:107], v[134:135]
	v_pk_add_f32 v[100:101], v[100:101], v[68:69]
	v_pk_add_f32 v[98:99], v[98:99], v[66:67]
	v_pk_add_f32 v[104:105], v[104:105], v[144:145]
	v_pk_add_f32 v[102:103], v[102:103], v[142:143]
	v_pk_add_f32 v[96:97], v[96:97], v[140:141]
	v_pk_add_f32 v[94:95], v[94:95], v[138:139]
	v_pk_add_f32 v[92:93], v[92:93], v[136:137]
	v_pk_add_f32 v[150:151], v[90:91], v[134:135]
	v_pk_add_f32 v[152:153], v[84:85], v[68:69]
	v_pk_add_f32 v[154:155], v[82:83], v[66:67]
	v_pk_add_f32 v[156:157], v[88:89], v[144:145]
	v_pk_add_f32 v[158:159], v[86:87], v[142:143]
	v_pk_add_f32 v[160:161], v[80:81], v[140:141]
	v_pk_add_f32 v[162:163], v[78:79], v[138:139]
	v_pk_add_f32 v[166:167], v[74:75], v[134:135]
	v_pk_add_f32 v[168:169], v[72:73], v[68:69]
	v_cvt_pk_f16_f32 v75, v128, v129
	v_cvt_pk_f16_f32 v73, v132, v133
	v_cvt_pk_f16_f32 v74, v126, v127
	v_cvt_pk_f16_f32 v72, v130, v131
	v_pk_add_f32 v[164:165], v[76:77], v[136:137]
	v_cvt_pk_f16_f32 v79, v116, v117
	v_cvt_pk_f16_f32 v77, v124, v125
	v_cvt_pk_f16_f32 v78, v114, v115
	v_cvt_pk_f16_f32 v76, v122, v123
	v_cvt_pk_f16_f32 v83, v112, v113
	v_cvt_pk_f16_f32 v81, v120, v121
	v_cvt_pk_f16_f32 v82, v110, v111
	v_cvt_pk_f16_f32 v80, v118, v119
	v_cvt_pk_f16_f32 v87, v100, v101
	v_cvt_pk_f16_f32 v85, v108, v109
	v_cvt_pk_f16_f32 v86, v98, v99
	v_cvt_pk_f16_f32 v84, v106, v107
	v_cvt_pk_f16_f32 v91, v96, v97
	v_cvt_pk_f16_f32 v89, v104, v105
	v_cvt_pk_f16_f32 v90, v94, v95
	v_cvt_pk_f16_f32 v88, v102, v103
	v_cvt_pk_f16_f32 v95, v152, v153
	v_cvt_pk_f16_f32 v93, v92, v93
	v_cvt_pk_f16_f32 v94, v154, v155
	v_cvt_pk_f16_f32 v92, v150, v151
	v_cvt_pk_f16_f32 v99, v160, v161
	v_cvt_pk_f16_f32 v97, v156, v157
	v_cvt_pk_f16_f32 v98, v162, v163
	v_cvt_pk_f16_f32 v96, v158, v159
	ds_write_b128 v1, v[72:75]
	ds_write_b128 v1, v[76:79] offset:256
	ds_write_b128 v1, v[80:83] offset:8448
	ds_write_b128 v1, v[84:87] offset:8704
	ds_write_b128 v1, v[88:91] offset:16896
	ds_write_b128 v1, v[92:95] offset:17152
	ds_write_b128 v1, v[96:99] offset:25344
	v_pk_add_f32 v[74:75], v[70:71], v[66:67]
	v_cvt_pk_f16_f32 v73, v168, v169
	v_cvt_pk_f16_f32 v71, v164, v165
	v_cvt_pk_f16_f32 v72, v74, v75
	v_cvt_pk_f16_f32 v70, v166, v167
	ds_write_b128 v1, v[70:73] offset:25600
	s_waitcnt lgkmcnt(0)
	s_barrier
	v_add_u32_e32 v74, s3, v170
	ds_read_b128 v[70:73], v148
	v_ashrrev_i32_e32 v75, 31, v74
	v_lshlrev_b64 v[74:75], 11, v[74:75]
	v_lshl_add_u64 v[74:75], s[24:25], 0, v[74:75]
	v_lshl_add_u64 v[74:75], v[74:75], 0, s[0:1]
	v_lshl_add_u64 v[78:79], v[74:75], 0, v[146:147]
	v_or_b32_e32 v80, 2, v170
	ds_read_b128 v[74:77], v148 offset:1056
	s_waitcnt lgkmcnt(1)
	global_store_dwordx4 v[78:79], v[70:73], off sc0 sc1
	v_or_b32_e32 v81, 4, v170
	v_or_b32_e32 v82, 6, v170
	v_add_u32_e32 v70, s3, v80
	v_ashrrev_i32_e32 v71, 31, v70
	v_lshlrev_b64 v[70:71], 11, v[70:71]
	v_lshl_add_u64 v[70:71], s[24:25], 0, v[70:71]
	v_lshl_add_u64 v[70:71], v[70:71], 0, s[0:1]
	v_lshl_add_u64 v[70:71], v[70:71], 0, v[146:147]
	s_waitcnt lgkmcnt(0)
	global_store_dwordx4 v[70:71], v[74:77], off sc0 sc1
	ds_read_b128 v[70:73], v148 offset:2112
	v_or_b32_e32 v83, 8, v170
	v_add_u32_e32 v74, s3, v81
	v_ashrrev_i32_e32 v75, 31, v74
	v_lshlrev_b64 v[74:75], 11, v[74:75]
	v_lshl_add_u64 v[74:75], s[24:25], 0, v[74:75]
	v_lshl_add_u64 v[74:75], v[74:75], 0, s[0:1]
	v_lshl_add_u64 v[78:79], v[74:75], 0, v[146:147]
	ds_read_b128 v[74:77], v148 offset:3168
	s_waitcnt lgkmcnt(1)
	global_store_dwordx4 v[78:79], v[70:73], off sc0 sc1
	v_or_b32_e32 v84, 10, v170
	v_or_b32_e32 v85, 12, v170
	v_add_u32_e32 v70, s3, v82
	v_ashrrev_i32_e32 v71, 31, v70
	v_lshlrev_b64 v[70:71], 11, v[70:71]
	v_lshl_add_u64 v[70:71], s[24:25], 0, v[70:71]
	v_lshl_add_u64 v[70:71], v[70:71], 0, s[0:1]
	v_lshl_add_u64 v[70:71], v[70:71], 0, v[146:147]
	s_waitcnt lgkmcnt(0)
	global_store_dwordx4 v[70:71], v[74:77], off sc0 sc1
	ds_read_b128 v[70:73], v148 offset:4224
	v_pk_add_f32 v[64:65], v[64:65], v[144:145]
	v_add_u32_e32 v74, s3, v83
	v_ashrrev_i32_e32 v75, 31, v74
	v_lshlrev_b64 v[74:75], 11, v[74:75]
	v_lshl_add_u64 v[74:75], s[24:25], 0, v[74:75]
	v_lshl_add_u64 v[74:75], v[74:75], 0, s[0:1]
	v_lshl_add_u64 v[78:79], v[74:75], 0, v[146:147]
	ds_read_b128 v[74:77], v148 offset:5280
	s_waitcnt lgkmcnt(1)
	global_store_dwordx4 v[78:79], v[70:73], off sc0 sc1
	v_pk_add_f32 v[62:63], v[62:63], v[142:143]
	v_pk_add_f32 v[60:61], v[60:61], v[140:141]
	v_add_u32_e32 v70, s3, v84
	v_ashrrev_i32_e32 v71, 31, v70
	v_lshlrev_b64 v[70:71], 11, v[70:71]
	v_lshl_add_u64 v[70:71], s[24:25], 0, v[70:71]
	v_lshl_add_u64 v[70:71], v[70:71], 0, s[0:1]
	v_lshl_add_u64 v[70:71], v[70:71], 0, v[146:147]
	s_waitcnt lgkmcnt(0)
	global_store_dwordx4 v[70:71], v[74:77], off sc0 sc1
	ds_read_b128 v[70:73], v148 offset:6336
	v_cvt_pk_f16_f32 v61, v60, v61
	v_add_u32_e32 v74, s3, v85
	v_ashrrev_i32_e32 v75, 31, v74
	v_lshlrev_b64 v[74:75], 11, v[74:75]
	v_lshl_add_u64 v[74:75], s[24:25], 0, v[74:75]
	v_lshl_add_u64 v[74:75], v[74:75], 0, s[0:1]
	v_lshl_add_u64 v[78:79], v[74:75], 0, v[146:147]
	ds_read_b128 v[74:77], v148 offset:7392
	s_waitcnt lgkmcnt(1)
	global_store_dwordx4 v[78:79], v[70:73], off sc0 sc1
	v_pk_add_f32 v[56:57], v[56:57], v[136:137]
	v_pk_add_f32 v[54:55], v[54:55], v[134:135]
	v_or_b32_e32 v72, 14, v170
	v_add_u32_e32 v70, s3, v72
	v_ashrrev_i32_e32 v71, 31, v70
	v_lshlrev_b64 v[70:71], 11, v[70:71]
	v_lshl_add_u64 v[70:71], s[24:25], 0, v[70:71]
	v_lshl_add_u64 v[70:71], v[70:71], 0, s[0:1]
	v_lshl_add_u64 v[70:71], v[70:71], 0, v[146:147]
	s_waitcnt lgkmcnt(0)
	global_store_dwordx4 v[70:71], v[74:77], off sc0 sc1
	v_pk_add_f32 v[70:71], v[58:59], v[138:139]
	v_cvt_pk_f16_f32 v59, v64, v65
	v_cvt_pk_f16_f32 v60, v70, v71
	v_cvt_pk_f16_f32 v58, v62, v63
	s_waitcnt lgkmcnt(0)
	s_barrier
	ds_write_b128 v1, v[58:61]
	v_pk_add_f32 v[48:49], v[48:49], v[68:69]
	v_pk_add_f32 v[58:59], v[46:47], v[66:67]
	v_cvt_pk_f16_f32 v49, v48, v49
	v_cvt_pk_f16_f32 v47, v56, v57
	v_cvt_pk_f16_f32 v48, v58, v59
	v_cvt_pk_f16_f32 v46, v54, v55
	ds_write_b128 v1, v[46:49] offset:256
	v_pk_add_f32 v[46:47], v[52:53], v[144:145]
	v_pk_add_f32 v[48:49], v[50:51], v[142:143]
	v_pk_add_f32 v[44:45], v[44:45], v[140:141]
	v_pk_add_f32 v[50:51], v[42:43], v[138:139]
	v_cvt_pk_f16_f32 v45, v44, v45
	v_cvt_pk_f16_f32 v43, v46, v47
	v_cvt_pk_f16_f32 v44, v50, v51
	v_cvt_pk_f16_f32 v42, v48, v49
	ds_write_b128 v1, v[42:45] offset:8448
	v_pk_add_f32 v[40:41], v[40:41], v[136:137]
	v_pk_add_f32 v[38:39], v[38:39], v[134:135]
	v_pk_add_f32 v[32:33], v[32:33], v[68:69]
	v_pk_add_f32 v[42:43], v[30:31], v[66:67]
	v_cvt_pk_f16_f32 v33, v32, v33
	v_cvt_pk_f16_f32 v31, v40, v41
	v_cvt_pk_f16_f32 v32, v42, v43
	v_cvt_pk_f16_f32 v30, v38, v39
	ds_write_b128 v1, v[30:33] offset:8704
	v_pk_add_f32 v[30:31], v[36:37], v[144:145]
	v_pk_add_f32 v[32:33], v[34:35], v[142:143]
	v_pk_add_f32 v[28:29], v[28:29], v[140:141]
	v_pk_add_f32 v[34:35], v[26:27], v[138:139]
	v_cvt_pk_f16_f32 v29, v28, v29
	v_cvt_pk_f16_f32 v27, v30, v31
	v_cvt_pk_f16_f32 v28, v34, v35
	v_cvt_pk_f16_f32 v26, v32, v33
	ds_write_b128 v1, v[26:29] offset:16896
	v_pk_add_f32 v[24:25], v[24:25], v[136:137]
	v_pk_add_f32 v[22:23], v[22:23], v[134:135]
	v_pk_add_f32 v[16:17], v[16:17], v[68:69]
	v_pk_add_f32 v[26:27], v[14:15], v[66:67]
	v_cvt_pk_f16_f32 v17, v16, v17
	v_cvt_pk_f16_f32 v15, v24, v25
	v_cvt_pk_f16_f32 v16, v26, v27
	v_cvt_pk_f16_f32 v14, v22, v23
	ds_write_b128 v1, v[14:17] offset:17152
	v_pk_add_f32 v[14:15], v[20:21], v[144:145]
	v_pk_add_f32 v[16:17], v[18:19], v[142:143]
	v_pk_add_f32 v[12:13], v[12:13], v[140:141]
	v_pk_add_f32 v[18:19], v[10:11], v[138:139]
	v_cvt_pk_f16_f32 v13, v12, v13
	v_cvt_pk_f16_f32 v11, v14, v15
	v_cvt_pk_f16_f32 v12, v18, v19
	v_cvt_pk_f16_f32 v10, v16, v17
	ds_write_b128 v1, v[10:13] offset:25344
	v_pk_add_f32 v[8:9], v[8:9], v[136:137]
	v_pk_add_f32 v[6:7], v[6:7], v[134:135]
	v_pk_add_f32 v[4:5], v[4:5], v[68:69]
	v_pk_add_f32 v[10:11], v[2:3], v[66:67]
	v_cvt_pk_f16_f32 v5, v4, v5
	v_cvt_pk_f16_f32 v3, v8, v9
	v_cvt_pk_f16_f32 v4, v10, v11
	v_cvt_pk_f16_f32 v2, v6, v7
	ds_write_b128 v1, v[2:5] offset:25600
	s_bitset1_b32 s3, 7
	s_waitcnt lgkmcnt(0)
	s_barrier
	v_add_u32_e32 v6, s3, v170
	ds_read_b128 v[2:5], v148
	v_ashrrev_i32_e32 v7, 31, v6
	v_lshlrev_b64 v[6:7], 11, v[6:7]
	v_lshl_add_u64 v[6:7], s[24:25], 0, v[6:7]
	v_lshl_add_u64 v[6:7], v[6:7], 0, s[0:1]
	v_lshl_add_u64 v[10:11], v[6:7], 0, v[146:147]
	ds_read_b128 v[6:9], v148 offset:1056
	s_waitcnt lgkmcnt(1)
	global_store_dwordx4 v[10:11], v[2:5], off sc0 sc1
	s_nop 1
	v_add_u32_e32 v2, s3, v80
	v_ashrrev_i32_e32 v3, 31, v2
	v_lshlrev_b64 v[2:3], 11, v[2:3]
	v_lshl_add_u64 v[2:3], s[24:25], 0, v[2:3]
	v_lshl_add_u64 v[2:3], v[2:3], 0, s[0:1]
	v_lshl_add_u64 v[2:3], v[2:3], 0, v[146:147]
	s_waitcnt lgkmcnt(0)
	global_store_dwordx4 v[2:3], v[6:9], off sc0 sc1
	ds_read_b128 v[2:5], v148 offset:2112
	s_nop 0
	v_add_u32_e32 v6, s3, v81
	v_ashrrev_i32_e32 v7, 31, v6
	v_lshlrev_b64 v[6:7], 11, v[6:7]
	v_lshl_add_u64 v[6:7], s[24:25], 0, v[6:7]
	v_lshl_add_u64 v[6:7], v[6:7], 0, s[0:1]
	v_lshl_add_u64 v[10:11], v[6:7], 0, v[146:147]
	ds_read_b128 v[6:9], v148 offset:3168
	s_waitcnt lgkmcnt(1)
	global_store_dwordx4 v[10:11], v[2:5], off sc0 sc1
	s_nop 1
	v_add_u32_e32 v2, s3, v82
	v_ashrrev_i32_e32 v3, 31, v2
	v_lshlrev_b64 v[2:3], 11, v[2:3]
	v_lshl_add_u64 v[2:3], s[24:25], 0, v[2:3]
	v_lshl_add_u64 v[2:3], v[2:3], 0, s[0:1]
	v_lshl_add_u64 v[2:3], v[2:3], 0, v[146:147]
	s_waitcnt lgkmcnt(0)
	global_store_dwordx4 v[2:3], v[6:9], off sc0 sc1
	ds_read_b128 v[2:5], v148 offset:4224
	s_nop 0
	v_add_u32_e32 v6, s3, v83
	v_ashrrev_i32_e32 v7, 31, v6
	v_lshlrev_b64 v[6:7], 11, v[6:7]
	v_lshl_add_u64 v[6:7], s[24:25], 0, v[6:7]
	v_lshl_add_u64 v[6:7], v[6:7], 0, s[0:1]
	v_lshl_add_u64 v[10:11], v[6:7], 0, v[146:147]
	ds_read_b128 v[6:9], v148 offset:5280
	s_waitcnt lgkmcnt(1)
	global_store_dwordx4 v[10:11], v[2:5], off sc0 sc1
	s_nop 1
	v_add_u32_e32 v2, s3, v84
	v_ashrrev_i32_e32 v3, 31, v2
	v_lshlrev_b64 v[2:3], 11, v[2:3]
	v_lshl_add_u64 v[2:3], s[24:25], 0, v[2:3]
	v_lshl_add_u64 v[2:3], v[2:3], 0, s[0:1]
	v_lshl_add_u64 v[2:3], v[2:3], 0, v[146:147]
	s_waitcnt lgkmcnt(0)
	global_store_dwordx4 v[2:3], v[6:9], off sc0 sc1
	ds_read_b128 v[2:5], v148 offset:6336
	s_nop 0
	v_add_u32_e32 v6, s3, v85
	v_ashrrev_i32_e32 v7, 31, v6
	v_lshlrev_b64 v[6:7], 11, v[6:7]
	v_lshl_add_u64 v[6:7], s[24:25], 0, v[6:7]
	v_lshl_add_u64 v[6:7], v[6:7], 0, s[0:1]
	v_lshl_add_u64 v[10:11], v[6:7], 0, v[146:147]
	ds_read_b128 v[6:9], v148 offset:7392
	s_waitcnt lgkmcnt(1)
	global_store_dwordx4 v[10:11], v[2:5], off sc0 sc1
	s_nop 1
	v_add_u32_e32 v2, s3, v72
	v_ashrrev_i32_e32 v3, 31, v2
	v_lshlrev_b64 v[2:3], 11, v[2:3]
	v_lshl_add_u64 v[2:3], s[24:25], 0, v[2:3]
	v_lshl_add_u64 v[2:3], v[2:3], 0, s[0:1]
	v_lshl_add_u64 v[2:3], v[2:3], 0, v[146:147]
	s_waitcnt lgkmcnt(0)
	global_store_dwordx4 v[2:3], v[6:9], off sc0 sc1
	s_waitcnt lgkmcnt(0)
	s_barrier
